# final_phase_handwritten_pipelined
# baseline (speedup 1.0000x reference)
.LBB0_1110:
	v_readlane_b32 s26, v253, 54
	v_readlane_b32 s27, v253, 55
	v_readlane_b32 s1, v253, 29
	v_readlane_b32 s22, v253, 50
	v_readlane_b32 s23, v253, 51
	v_readlane_b32 s24, v253, 52
	v_readlane_b32 s25, v253, 53
	v_and_b32_e32 v104, 63, v0
	v_lshlrev_b32_e32 v105, 3, v104
	v_lshlrev_b32_e32 v106, 2, v104
	v_lshlrev_b32_e32 v107, 4, v104
	v_mov_b32_e32 v108, 0x358637bd
	v_mov_b32_e32 v109, 0x260
	s_mov_b32 s35, 0xf800000
	s_lshl_b32 s0, s5, 3
	s_add_i32 s2, s0, s1
	s_lshl_b32 s20, s37, 3
	s_lshl_b32 s21, s37, 4
	s_add_u32 s4, s26, 0x400000
	s_addc_u32 s5, s27, 0
	s_add_u32 s6, s26, 0x4a000000
	s_addc_u32 s7, s27, 0
	s_add_u32 s8, s26, 0x27000000
	s_addc_u32 s9, s27, 0
	s_cmp_lt_i32 s2, 0x8000
	s_cbranch_scc0 .LBB0_1150
	global_load_dwordx4 v[112:115], v107, s[22:23]
	global_load_dwordx4 v[116:119], v107, s[22:23] offset:1024
	global_load_dwordx4 v[120:123], v107, s[22:23] offset:2048
	global_load_dwordx4 v[124:127], v107, s[22:23] offset:3072
	s_lshl_b32 s10, s2, 11
	s_add_u32 s10, s6, s10
	s_addc_u32 s11, s7, 0
	s_lshl_b32 s12, s2, 6
	s_add_u32 s12, s4, s12
	s_addc_u32 s13, s5, 0
	global_load_dwordx2 v[0:1], v105, s[10:11]
	global_load_dwordx2 v[2:3], v105, s[10:11] offset:512
	global_load_dwordx2 v[4:5], v105, s[10:11] offset:1024
	global_load_dwordx2 v[6:7], v105, s[10:11] offset:1536
	global_load_dword v16, v106, s[12:13]
	s_add_i32 s34, s2, s20
	s_cmp_lt_i32 s34, 0x8000
	s_cbranch_scc0 .Lfin_pf_first
	s_lshl_b32 s10, s34, 11
	s_add_u32 s10, s6, s10
	s_addc_u32 s11, s7, 0
	s_lshl_b32 s12, s34, 6
	s_add_u32 s12, s4, s12
	s_addc_u32 s13, s5, 0
	global_load_dwordx2 v[8:9], v105, s[10:11]
	global_load_dwordx2 v[10:11], v105, s[10:11] offset:512
	global_load_dwordx2 v[12:13], v105, s[10:11] offset:1024
	global_load_dwordx2 v[14:15], v105, s[10:11] offset:1536
	global_load_dword v17, v106, s[12:13]
.Lfin_pf_first:
	s_mov_b32 s28, 0
.Lfin_loop:
	s_add_i32 s3, s2, s20
	s_cmp_lt_i32 s3, 0x8000
	s_cselect_b32 s29, 1, 0
	s_cmp_lg_u32 s28, 0
	s_cbranch_scc1 .Lfin_nowait
	s_waitcnt vmcnt(0)
.Lfin_nowait:
	v_lshlrev_b32_e32 v32, 16, v0
	v_and_b32_e32 v33, 0xffff0000, v0
	v_lshlrev_b32_e32 v34, 16, v1
	v_and_b32_e32 v35, 0xffff0000, v1
	v_lshlrev_b32_e32 v36, 16, v2
	v_and_b32_e32 v37, 0xffff0000, v2
	v_lshlrev_b32_e32 v38, 16, v3
	v_and_b32_e32 v39, 0xffff0000, v3
	v_lshlrev_b32_e32 v40, 16, v4
	v_and_b32_e32 v41, 0xffff0000, v4
	v_lshlrev_b32_e32 v42, 16, v5
	v_and_b32_e32 v43, 0xffff0000, v5
	v_lshlrev_b32_e32 v44, 16, v6
	v_and_b32_e32 v45, 0xffff0000, v6
	v_lshlrev_b32_e32 v46, 16, v7
	v_and_b32_e32 v47, 0xffff0000, v7
	v_lshlrev_b32_e32 v48, 16, v8
	v_and_b32_e32 v49, 0xffff0000, v8
	v_lshlrev_b32_e32 v50, 16, v9
	v_and_b32_e32 v51, 0xffff0000, v9
	v_lshlrev_b32_e32 v52, 16, v10
	v_and_b32_e32 v53, 0xffff0000, v10
	v_lshlrev_b32_e32 v54, 16, v11
	v_and_b32_e32 v55, 0xffff0000, v11
	v_lshlrev_b32_e32 v56, 16, v12
	v_and_b32_e32 v57, 0xffff0000, v12
	v_lshlrev_b32_e32 v58, 16, v13
	v_and_b32_e32 v59, 0xffff0000, v13
	v_lshlrev_b32_e32 v60, 16, v14
	v_and_b32_e32 v61, 0xffff0000, v14
	v_lshlrev_b32_e32 v62, 16, v15
	v_and_b32_e32 v63, 0xffff0000, v15
	v_mov_b32_e32 v18, v16
	v_mov_b32_e32 v19, v17
	v_cmp_lt_i32_e32 vcc, -1, v18
	s_and_b32 s30, vcc_lo, 0xffff
	v_cmp_lt_i32_e32 vcc, -1, v19
	s_and_b32 s31, vcc_lo, 0xffff
	s_cmp_eq_u32 s29, 0
	s_cselect_b32 s31, 0, s31
	s_add_i32 s33, s2, s21
	s_cmp_lt_i32 s33, 0x8000
	s_cbranch_scc0 .Lfin_pf_next
	s_lshl_b32 s10, s33, 11
	s_add_u32 s10, s6, s10
	s_addc_u32 s11, s7, 0
	s_lshl_b32 s12, s33, 6
	s_add_u32 s12, s4, s12
	s_addc_u32 s13, s5, 0
	global_load_dwordx2 v[0:1], v105, s[10:11]
	global_load_dwordx2 v[2:3], v105, s[10:11] offset:512
	global_load_dwordx2 v[4:5], v105, s[10:11] offset:1024
	global_load_dwordx2 v[6:7], v105, s[10:11] offset:1536
	global_load_dword v16, v106, s[12:13]
	s_add_i32 s34, s33, s20
	s_cmp_lt_i32 s34, 0x8000
	s_cbranch_scc0 .Lfin_pf_next
	s_lshl_b32 s10, s34, 11
	s_add_u32 s10, s6, s10
	s_addc_u32 s11, s7, 0
	s_lshl_b32 s12, s34, 6
	s_add_u32 s12, s4, s12
	s_addc_u32 s13, s5, 0
	global_load_dwordx2 v[8:9], v105, s[10:11]
	global_load_dwordx2 v[10:11], v105, s[10:11] offset:512
	global_load_dwordx2 v[12:13], v105, s[10:11] offset:1024
	global_load_dwordx2 v[14:15], v105, s[10:11] offset:1536
	global_load_dword v17, v106, s[12:13]
.Lfin_pf_next:
	s_mov_b32 s28, 0
	s_or_b32 s0, s30, s31
	s_cmp_eq_u32 s0, 0
	s_cbranch_scc1 .Lfin_rounds_done
.Lfin_round:
	s_add_i32 s28, s28, 1
	s_mov_b32 s36, 0
	s_cmp_eq_u32 s30, 0
	s_cbranch_scc1 .Lfin_iss_A_done
	s_ff1_i32_b32 s14, s30
	s_bitset0_b32 s30, s14
	v_readlane_b32 s15, v18, s14
	s_lshl_b32 s15, s15, 11
	s_add_u32 s16, s8, s15
	s_addc_u32 s17, s9, 0
	global_load_dwordx2 v[128:129], v105, s[16:17]
	global_load_dwordx2 v[130:131], v105, s[16:17] offset:512
	global_load_dwordx2 v[132:133], v105, s[16:17] offset:1024
	global_load_dwordx2 v[134:135], v105, s[16:17] offset:1536
	s_bitset1_b32 s36, 0
	s_cmp_eq_u32 s30, 0
	s_cbranch_scc1 .Lfin_iss_A_done
	s_ff1_i32_b32 s14, s30
	s_bitset0_b32 s30, s14
	v_readlane_b32 s15, v18, s14
	s_lshl_b32 s15, s15, 11
	s_add_u32 s16, s8, s15
	s_addc_u32 s17, s9, 0
	global_load_dwordx2 v[136:137], v105, s[16:17]
	global_load_dwordx2 v[138:139], v105, s[16:17] offset:512
	global_load_dwordx2 v[140:141], v105, s[16:17] offset:1024
	global_load_dwordx2 v[142:143], v105, s[16:17] offset:1536
	s_bitset1_b32 s36, 1
	s_cmp_eq_u32 s30, 0
	s_cbranch_scc1 .Lfin_iss_A_done
	s_ff1_i32_b32 s14, s30
	s_bitset0_b32 s30, s14
	v_readlane_b32 s15, v18, s14
	s_lshl_b32 s15, s15, 11
	s_add_u32 s16, s8, s15
	s_addc_u32 s17, s9, 0
	global_load_dwordx2 v[144:145], v105, s[16:17]
	global_load_dwordx2 v[146:147], v105, s[16:17] offset:512
	global_load_dwordx2 v[148:149], v105, s[16:17] offset:1024
	global_load_dwordx2 v[150:151], v105, s[16:17] offset:1536
	s_bitset1_b32 s36, 2
	s_cmp_eq_u32 s30, 0
	s_cbranch_scc1 .Lfin_iss_A_done
	s_ff1_i32_b32 s14, s30
	s_bitset0_b32 s30, s14
	v_readlane_b32 s15, v18, s14
	s_lshl_b32 s15, s15, 11
	s_add_u32 s16, s8, s15
	s_addc_u32 s17, s9, 0
	global_load_dwordx2 v[152:153], v105, s[16:17]
	global_load_dwordx2 v[154:155], v105, s[16:17] offset:512
	global_load_dwordx2 v[156:157], v105, s[16:17] offset:1024
	global_load_dwordx2 v[158:159], v105, s[16:17] offset:1536
	s_bitset1_b32 s36, 3
.Lfin_iss_A_done:
	s_cmp_eq_u32 s31, 0
	s_cbranch_scc1 .Lfin_iss_B_done
	s_ff1_i32_b32 s14, s31
	s_bitset0_b32 s31, s14
	v_readlane_b32 s15, v19, s14
	s_lshl_b32 s15, s15, 11
	s_add_u32 s16, s8, s15
	s_addc_u32 s17, s9, 0
	global_load_dwordx2 v[160:161], v105, s[16:17]
	global_load_dwordx2 v[162:163], v105, s[16:17] offset:512
	global_load_dwordx2 v[164:165], v105, s[16:17] offset:1024
	global_load_dwordx2 v[166:167], v105, s[16:17] offset:1536
	s_bitset1_b32 s36, 4
	s_cmp_eq_u32 s31, 0
	s_cbranch_scc1 .Lfin_iss_B_done
	s_ff1_i32_b32 s14, s31
	s_bitset0_b32 s31, s14
	v_readlane_b32 s15, v19, s14
	s_lshl_b32 s15, s15, 11
	s_add_u32 s16, s8, s15
	s_addc_u32 s17, s9, 0
	global_load_dwordx2 v[168:169], v105, s[16:17]
	global_load_dwordx2 v[170:171], v105, s[16:17] offset:512
	global_load_dwordx2 v[172:173], v105, s[16:17] offset:1024
	global_load_dwordx2 v[174:175], v105, s[16:17] offset:1536
	s_bitset1_b32 s36, 5
	s_cmp_eq_u32 s31, 0
	s_cbranch_scc1 .Lfin_iss_B_done
	s_ff1_i32_b32 s14, s31
	s_bitset0_b32 s31, s14
	v_readlane_b32 s15, v19, s14
	s_lshl_b32 s15, s15, 11
	s_add_u32 s16, s8, s15
	s_addc_u32 s17, s9, 0
	global_load_dwordx2 v[176:177], v105, s[16:17]
	global_load_dwordx2 v[178:179], v105, s[16:17] offset:512
	global_load_dwordx2 v[180:181], v105, s[16:17] offset:1024
	global_load_dwordx2 v[182:183], v105, s[16:17] offset:1536
	s_bitset1_b32 s36, 6
	s_cmp_eq_u32 s31, 0
	s_cbranch_scc1 .Lfin_iss_B_done
	s_ff1_i32_b32 s14, s31
	s_bitset0_b32 s31, s14
	v_readlane_b32 s15, v19, s14
	s_lshl_b32 s15, s15, 11
	s_add_u32 s16, s8, s15
	s_addc_u32 s17, s9, 0
	global_load_dwordx2 v[184:185], v105, s[16:17]
	global_load_dwordx2 v[186:187], v105, s[16:17] offset:512
	global_load_dwordx2 v[188:189], v105, s[16:17] offset:1024
	global_load_dwordx2 v[190:191], v105, s[16:17] offset:1536
	s_bitset1_b32 s36, 7
.Lfin_iss_B_done:
	s_waitcnt vmcnt(0)
	s_bitcmp1_b32 s36, 0
	s_cbranch_scc0 .Lfin_add_skip_0
	v_lshlrev_b32_e32 v64, 16, v128
	v_and_b32_e32 v65, 0xffff0000, v128
	v_pk_add_f32 v[32:33], v[32:33], v[64:65]
	v_lshlrev_b32_e32 v66, 16, v129
	v_and_b32_e32 v67, 0xffff0000, v129
	v_pk_add_f32 v[34:35], v[34:35], v[66:67]
	v_lshlrev_b32_e32 v68, 16, v130
	v_and_b32_e32 v69, 0xffff0000, v130
	v_pk_add_f32 v[36:37], v[36:37], v[68:69]
	v_lshlrev_b32_e32 v70, 16, v131
	v_and_b32_e32 v71, 0xffff0000, v131
	v_pk_add_f32 v[38:39], v[38:39], v[70:71]
	v_lshlrev_b32_e32 v72, 16, v132
	v_and_b32_e32 v73, 0xffff0000, v132
	v_pk_add_f32 v[40:41], v[40:41], v[72:73]
	v_lshlrev_b32_e32 v74, 16, v133
	v_and_b32_e32 v75, 0xffff0000, v133
	v_pk_add_f32 v[42:43], v[42:43], v[74:75]
	v_lshlrev_b32_e32 v76, 16, v134
	v_and_b32_e32 v77, 0xffff0000, v134
	v_pk_add_f32 v[44:45], v[44:45], v[76:77]
	v_lshlrev_b32_e32 v78, 16, v135
	v_and_b32_e32 v79, 0xffff0000, v135
	v_pk_add_f32 v[46:47], v[46:47], v[78:79]
.Lfin_add_skip_0:
	s_bitcmp1_b32 s36, 1
	s_cbranch_scc0 .Lfin_add_skip_1
	v_lshlrev_b32_e32 v64, 16, v136
	v_and_b32_e32 v65, 0xffff0000, v136
	v_pk_add_f32 v[32:33], v[32:33], v[64:65]
	v_lshlrev_b32_e32 v66, 16, v137
	v_and_b32_e32 v67, 0xffff0000, v137
	v_pk_add_f32 v[34:35], v[34:35], v[66:67]
	v_lshlrev_b32_e32 v68, 16, v138
	v_and_b32_e32 v69, 0xffff0000, v138
	v_pk_add_f32 v[36:37], v[36:37], v[68:69]
	v_lshlrev_b32_e32 v70, 16, v139
	v_and_b32_e32 v71, 0xffff0000, v139
	v_pk_add_f32 v[38:39], v[38:39], v[70:71]
	v_lshlrev_b32_e32 v72, 16, v140
	v_and_b32_e32 v73, 0xffff0000, v140
	v_pk_add_f32 v[40:41], v[40:41], v[72:73]
	v_lshlrev_b32_e32 v74, 16, v141
	v_and_b32_e32 v75, 0xffff0000, v141
	v_pk_add_f32 v[42:43], v[42:43], v[74:75]
	v_lshlrev_b32_e32 v76, 16, v142
	v_and_b32_e32 v77, 0xffff0000, v142
	v_pk_add_f32 v[44:45], v[44:45], v[76:77]
	v_lshlrev_b32_e32 v78, 16, v143
	v_and_b32_e32 v79, 0xffff0000, v143
	v_pk_add_f32 v[46:47], v[46:47], v[78:79]
.Lfin_add_skip_1:
	s_bitcmp1_b32 s36, 2
	s_cbranch_scc0 .Lfin_add_skip_2
	v_lshlrev_b32_e32 v64, 16, v144
	v_and_b32_e32 v65, 0xffff0000, v144
	v_pk_add_f32 v[32:33], v[32:33], v[64:65]
	v_lshlrev_b32_e32 v66, 16, v145
	v_and_b32_e32 v67, 0xffff0000, v145
	v_pk_add_f32 v[34:35], v[34:35], v[66:67]
	v_lshlrev_b32_e32 v68, 16, v146
	v_and_b32_e32 v69, 0xffff0000, v146
	v_pk_add_f32 v[36:37], v[36:37], v[68:69]
	v_lshlrev_b32_e32 v70, 16, v147
	v_and_b32_e32 v71, 0xffff0000, v147
	v_pk_add_f32 v[38:39], v[38:39], v[70:71]
	v_lshlrev_b32_e32 v72, 16, v148
	v_and_b32_e32 v73, 0xffff0000, v148
	v_pk_add_f32 v[40:41], v[40:41], v[72:73]
	v_lshlrev_b32_e32 v74, 16, v149
	v_and_b32_e32 v75, 0xffff0000, v149
	v_pk_add_f32 v[42:43], v[42:43], v[74:75]
	v_lshlrev_b32_e32 v76, 16, v150
	v_and_b32_e32 v77, 0xffff0000, v150
	v_pk_add_f32 v[44:45], v[44:45], v[76:77]
	v_lshlrev_b32_e32 v78, 16, v151
	v_and_b32_e32 v79, 0xffff0000, v151
	v_pk_add_f32 v[46:47], v[46:47], v[78:79]
.Lfin_add_skip_2:
	s_bitcmp1_b32 s36, 3
	s_cbranch_scc0 .Lfin_add_skip_3
	v_lshlrev_b32_e32 v64, 16, v152
	v_and_b32_e32 v65, 0xffff0000, v152
	v_pk_add_f32 v[32:33], v[32:33], v[64:65]
	v_lshlrev_b32_e32 v66, 16, v153
	v_and_b32_e32 v67, 0xffff0000, v153
	v_pk_add_f32 v[34:35], v[34:35], v[66:67]
	v_lshlrev_b32_e32 v68, 16, v154
	v_and_b32_e32 v69, 0xffff0000, v154
	v_pk_add_f32 v[36:37], v[36:37], v[68:69]
	v_lshlrev_b32_e32 v70, 16, v155
	v_and_b32_e32 v71, 0xffff0000, v155
	v_pk_add_f32 v[38:39], v[38:39], v[70:71]
	v_lshlrev_b32_e32 v72, 16, v156
	v_and_b32_e32 v73, 0xffff0000, v156
	v_pk_add_f32 v[40:41], v[40:41], v[72:73]
	v_lshlrev_b32_e32 v74, 16, v157
	v_and_b32_e32 v75, 0xffff0000, v157
	v_pk_add_f32 v[42:43], v[42:43], v[74:75]
	v_lshlrev_b32_e32 v76, 16, v158
	v_and_b32_e32 v77, 0xffff0000, v158
	v_pk_add_f32 v[44:45], v[44:45], v[76:77]
	v_lshlrev_b32_e32 v78, 16, v159
	v_and_b32_e32 v79, 0xffff0000, v159
	v_pk_add_f32 v[46:47], v[46:47], v[78:79]
.Lfin_add_skip_3:
	s_bitcmp1_b32 s36, 4
	s_cbranch_scc0 .Lfin_add_skip_4
	v_lshlrev_b32_e32 v64, 16, v160
	v_and_b32_e32 v65, 0xffff0000, v160
	v_pk_add_f32 v[48:49], v[48:49], v[64:65]
	v_lshlrev_b32_e32 v66, 16, v161
	v_and_b32_e32 v67, 0xffff0000, v161
	v_pk_add_f32 v[50:51], v[50:51], v[66:67]
	v_lshlrev_b32_e32 v68, 16, v162
	v_and_b32_e32 v69, 0xffff0000, v162
	v_pk_add_f32 v[52:53], v[52:53], v[68:69]
	v_lshlrev_b32_e32 v70, 16, v163
	v_and_b32_e32 v71, 0xffff0000, v163
	v_pk_add_f32 v[54:55], v[54:55], v[70:71]
	v_lshlrev_b32_e32 v72, 16, v164
	v_and_b32_e32 v73, 0xffff0000, v164
	v_pk_add_f32 v[56:57], v[56:57], v[72:73]
	v_lshlrev_b32_e32 v74, 16, v165
	v_and_b32_e32 v75, 0xffff0000, v165
	v_pk_add_f32 v[58:59], v[58:59], v[74:75]
	v_lshlrev_b32_e32 v76, 16, v166
	v_and_b32_e32 v77, 0xffff0000, v166
	v_pk_add_f32 v[60:61], v[60:61], v[76:77]
	v_lshlrev_b32_e32 v78, 16, v167
	v_and_b32_e32 v79, 0xffff0000, v167
	v_pk_add_f32 v[62:63], v[62:63], v[78:79]
.Lfin_add_skip_4:
	s_bitcmp1_b32 s36, 5
	s_cbranch_scc0 .Lfin_add_skip_5
	v_lshlrev_b32_e32 v64, 16, v168
	v_and_b32_e32 v65, 0xffff0000, v168
	v_pk_add_f32 v[48:49], v[48:49], v[64:65]
	v_lshlrev_b32_e32 v66, 16, v169
	v_and_b32_e32 v67, 0xffff0000, v169
	v_pk_add_f32 v[50:51], v[50:51], v[66:67]
	v_lshlrev_b32_e32 v68, 16, v170
	v_and_b32_e32 v69, 0xffff0000, v170
	v_pk_add_f32 v[52:53], v[52:53], v[68:69]
	v_lshlrev_b32_e32 v70, 16, v171
	v_and_b32_e32 v71, 0xffff0000, v171
	v_pk_add_f32 v[54:55], v[54:55], v[70:71]
	v_lshlrev_b32_e32 v72, 16, v172
	v_and_b32_e32 v73, 0xffff0000, v172
	v_pk_add_f32 v[56:57], v[56:57], v[72:73]
	v_lshlrev_b32_e32 v74, 16, v173
	v_and_b32_e32 v75, 0xffff0000, v173
	v_pk_add_f32 v[58:59], v[58:59], v[74:75]
	v_lshlrev_b32_e32 v76, 16, v174
	v_and_b32_e32 v77, 0xffff0000, v174
	v_pk_add_f32 v[60:61], v[60:61], v[76:77]
	v_lshlrev_b32_e32 v78, 16, v175
	v_and_b32_e32 v79, 0xffff0000, v175
	v_pk_add_f32 v[62:63], v[62:63], v[78:79]
.Lfin_add_skip_5:
	s_bitcmp1_b32 s36, 6
	s_cbranch_scc0 .Lfin_add_skip_6
	v_lshlrev_b32_e32 v64, 16, v176
	v_and_b32_e32 v65, 0xffff0000, v176
	v_pk_add_f32 v[48:49], v[48:49], v[64:65]
	v_lshlrev_b32_e32 v66, 16, v177
	v_and_b32_e32 v67, 0xffff0000, v177
	v_pk_add_f32 v[50:51], v[50:51], v[66:67]
	v_lshlrev_b32_e32 v68, 16, v178
	v_and_b32_e32 v69, 0xffff0000, v178
	v_pk_add_f32 v[52:53], v[52:53], v[68:69]
	v_lshlrev_b32_e32 v70, 16, v179
	v_and_b32_e32 v71, 0xffff0000, v179
	v_pk_add_f32 v[54:55], v[54:55], v[70:71]
	v_lshlrev_b32_e32 v72, 16, v180
	v_and_b32_e32 v73, 0xffff0000, v180
	v_pk_add_f32 v[56:57], v[56:57], v[72:73]
	v_lshlrev_b32_e32 v74, 16, v181
	v_and_b32_e32 v75, 0xffff0000, v181
	v_pk_add_f32 v[58:59], v[58:59], v[74:75]
	v_lshlrev_b32_e32 v76, 16, v182
	v_and_b32_e32 v77, 0xffff0000, v182
	v_pk_add_f32 v[60:61], v[60:61], v[76:77]
	v_lshlrev_b32_e32 v78, 16, v183
	v_and_b32_e32 v79, 0xffff0000, v183
	v_pk_add_f32 v[62:63], v[62:63], v[78:79]
.Lfin_add_skip_6:
	s_bitcmp1_b32 s36, 7
	s_cbranch_scc0 .Lfin_add_skip_7
	v_lshlrev_b32_e32 v64, 16, v184
	v_and_b32_e32 v65, 0xffff0000, v184
	v_pk_add_f32 v[48:49], v[48:49], v[64:65]
	v_lshlrev_b32_e32 v66, 16, v185
	v_and_b32_e32 v67, 0xffff0000, v185
	v_pk_add_f32 v[50:51], v[50:51], v[66:67]
	v_lshlrev_b32_e32 v68, 16, v186
	v_and_b32_e32 v69, 0xffff0000, v186
	v_pk_add_f32 v[52:53], v[52:53], v[68:69]
	v_lshlrev_b32_e32 v70, 16, v187
	v_and_b32_e32 v71, 0xffff0000, v187
	v_pk_add_f32 v[54:55], v[54:55], v[70:71]
	v_lshlrev_b32_e32 v72, 16, v188
	v_and_b32_e32 v73, 0xffff0000, v188
	v_pk_add_f32 v[56:57], v[56:57], v[72:73]
	v_lshlrev_b32_e32 v74, 16, v189
	v_and_b32_e32 v75, 0xffff0000, v189
	v_pk_add_f32 v[58:59], v[58:59], v[74:75]
	v_lshlrev_b32_e32 v76, 16, v190
	v_and_b32_e32 v77, 0xffff0000, v190
	v_pk_add_f32 v[60:61], v[60:61], v[76:77]
	v_lshlrev_b32_e32 v78, 16, v191
	v_and_b32_e32 v79, 0xffff0000, v191
	v_pk_add_f32 v[62:63], v[62:63], v[78:79]
.Lfin_add_skip_7:
	s_or_b32 s0, s30, s31
	s_cmp_lg_u32 s0, 0
	s_cbranch_scc1 .Lfin_round
.Lfin_rounds_done:
	v_mul_f32_e32 v94, v33, v33
	v_mul_f32_e32 v95, v35, v35
	v_mul_f32_e32 v96, v37, v37
	v_mul_f32_e32 v97, v39, v39
	v_mul_f32_e32 v98, v41, v41
	v_mul_f32_e32 v99, v43, v43
	v_mul_f32_e32 v100, v45, v45
	v_mul_f32_e32 v101, v47, v47
	v_fmac_f32_e32 v94, v32, v32
	v_fmac_f32_e32 v95, v34, v34
	v_fmac_f32_e32 v96, v36, v36
	v_fmac_f32_e32 v97, v38, v38
	v_fmac_f32_e32 v98, v40, v40
	v_fmac_f32_e32 v99, v42, v42
	v_fmac_f32_e32 v100, v44, v44
	v_fmac_f32_e32 v101, v46, v46
	v_add_f32_e32 v94, v94, v95
	v_add_f32_e32 v96, v96, v97
	v_add_f32_e32 v98, v98, v99
	v_add_f32_e32 v100, v100, v101
	v_add_f32_e32 v84, v96, v94
	v_add_f32_e32 v84, v98, v84
	v_add_f32_e32 v84, v100, v84
	s_lshl_b32 s10, s2, 12
	s_add_u32 s10, s24, s10
	s_addc_u32 s11, s25, 0
	s_nop 1
	v_add_f32_dpp v84, v84, v84 quad_perm:[1,0,3,2] row_mask:0xf bank_mask:0xf bound_ctrl:1
	s_nop 1
	v_add_f32_dpp v84, v84, v84 quad_perm:[2,3,0,1] row_mask:0xf bank_mask:0xf bound_ctrl:1
	s_nop 1
	v_add_f32_dpp v84, v84, v84 row_half_mirror row_mask:0xf bank_mask:0xf bound_ctrl:1
	s_nop 1
	v_add_f32_dpp v84, v84, v84 row_mirror row_mask:0xf bank_mask:0xf bound_ctrl:1
	v_mov_b32_e32 v85, v84
	s_nop 1
	v_permlane16_swap_b32_e32 v84, v85
	v_add_f32_e32 v84, v84, v85
	v_mov_b32_e32 v85, v84
	s_nop 1
	v_permlane32_swap_b32_e32 v84, v85
	v_add_f32_e32 v84, v84, v85
	v_fmamk_f32 v84, v84, 0x3a800000, v108
	v_mul_f32_e32 v85, 0x4f800000, v84
	v_cmp_gt_f32_e32 vcc, s35, v84
	s_nop 1
	v_cndmask_b32_e32 v84, v84, v85, vcc
	v_sqrt_f32_e32 v85, v84
	s_nop 0
	v_add_u32_e32 v86, -1, v85
	v_add_u32_e32 v91, 1, v85
	v_fma_f32 v89, -v86, v85, v84
	v_fma_f32 v90, -v91, v85, v84
	v_cmp_ge_f32_e64 s[12:13], 0, v89
	s_nop 1
	v_cndmask_b32_e64 v85, v85, v86, s[12:13]
	v_cmp_lt_f32_e64 s[12:13], 0, v90
	s_nop 1
	v_cndmask_b32_e64 v85, v85, v91, s[12:13]
	v_mul_f32_e32 v86, 0x37800000, v85
	v_cndmask_b32_e32 v85, v85, v86, vcc
	v_cmp_class_f32_e32 vcc, v84, v109
	s_nop 1
	v_cndmask_b32_e32 v84, v85, v84, vcc
	v_div_scale_f32 v88, s[12:13], v84, v84, 1.0
	v_rcp_f32_e32 v89, v88
	v_div_scale_f32 v90, vcc, 1.0, v84, 1.0
	s_nop 0
	v_fma_f32 v91, -v88, v89, 1.0
	v_fmac_f32_e32 v89, v91, v89
	v_mul_f32_e32 v91, v90, v89
	v_fma_f32 v92, -v88, v91, v90
	v_fmac_f32_e32 v91, v92, v89
	v_fma_f32 v88, -v88, v91, v90
	v_div_fmas_f32 v88, v88, v89, v91
	v_div_fixup_f32 v88, v88, v84, 1.0
	v_pk_mul_f32 v[32:33], v[88:89], v[32:33] op_sel_hi:[0,1]
	v_pk_mul_f32 v[34:35], v[88:89], v[34:35] op_sel_hi:[0,1]
	v_pk_mul_f32 v[36:37], v[88:89], v[36:37] op_sel_hi:[0,1]
	v_pk_mul_f32 v[38:39], v[88:89], v[38:39] op_sel_hi:[0,1]
	v_pk_mul_f32 v[40:41], v[88:89], v[40:41] op_sel_hi:[0,1]
	v_pk_mul_f32 v[42:43], v[88:89], v[42:43] op_sel_hi:[0,1]
	v_pk_mul_f32 v[44:45], v[88:89], v[44:45] op_sel_hi:[0,1]
	v_pk_mul_f32 v[46:47], v[88:89], v[46:47] op_sel_hi:[0,1]
	v_pk_mul_f32 v[32:33], v[112:113], v[32:33]
	v_pk_mul_f32 v[34:35], v[114:115], v[34:35]
	global_store_dwordx4 v107, v[32:35], s[10:11]
	v_pk_mul_f32 v[36:37], v[116:117], v[36:37]
	v_pk_mul_f32 v[38:39], v[118:119], v[38:39]
	global_store_dwordx4 v107, v[36:39], s[10:11] offset:1024
	v_pk_mul_f32 v[40:41], v[120:121], v[40:41]
	v_pk_mul_f32 v[42:43], v[122:123], v[42:43]
	global_store_dwordx4 v107, v[40:43], s[10:11] offset:2048
	v_pk_mul_f32 v[44:45], v[124:125], v[44:45]
	v_pk_mul_f32 v[46:47], v[126:127], v[46:47]
	global_store_dwordx4 v107, v[44:47], s[10:11] offset:3072
	s_cmp_eq_u32 s29, 0
	s_cbranch_scc1 .Lfin_skipB
	v_mul_f32_e32 v94, v49, v49
	v_mul_f32_e32 v95, v51, v51
	v_mul_f32_e32 v96, v53, v53
	v_mul_f32_e32 v97, v55, v55
	v_mul_f32_e32 v98, v57, v57
	v_mul_f32_e32 v99, v59, v59
	v_mul_f32_e32 v100, v61, v61
	v_mul_f32_e32 v101, v63, v63
	v_fmac_f32_e32 v94, v48, v48
	v_fmac_f32_e32 v95, v50, v50
	v_fmac_f32_e32 v96, v52, v52
	v_fmac_f32_e32 v97, v54, v54
	v_fmac_f32_e32 v98, v56, v56
	v_fmac_f32_e32 v99, v58, v58
	v_fmac_f32_e32 v100, v60, v60
	v_fmac_f32_e32 v101, v62, v62
	v_add_f32_e32 v94, v94, v95
	v_add_f32_e32 v96, v96, v97
	v_add_f32_e32 v98, v98, v99
	v_add_f32_e32 v100, v100, v101
	v_add_f32_e32 v84, v96, v94
	v_add_f32_e32 v84, v98, v84
	v_add_f32_e32 v84, v100, v84
	s_lshl_b32 s10, s3, 12
	s_add_u32 s10, s24, s10
	s_addc_u32 s11, s25, 0
	s_nop 1
	v_add_f32_dpp v84, v84, v84 quad_perm:[1,0,3,2] row_mask:0xf bank_mask:0xf bound_ctrl:1
	s_nop 1
	v_add_f32_dpp v84, v84, v84 quad_perm:[2,3,0,1] row_mask:0xf bank_mask:0xf bound_ctrl:1
	s_nop 1
	v_add_f32_dpp v84, v84, v84 row_half_mirror row_mask:0xf bank_mask:0xf bound_ctrl:1
	s_nop 1
	v_add_f32_dpp v84, v84, v84 row_mirror row_mask:0xf bank_mask:0xf bound_ctrl:1
	v_mov_b32_e32 v85, v84
	s_nop 1
	v_permlane16_swap_b32_e32 v84, v85
	v_add_f32_e32 v84, v84, v85
	v_mov_b32_e32 v85, v84
	s_nop 1
	v_permlane32_swap_b32_e32 v84, v85
	v_add_f32_e32 v84, v84, v85
	v_fmamk_f32 v84, v84, 0x3a800000, v108
	v_mul_f32_e32 v85, 0x4f800000, v84
	v_cmp_gt_f32_e32 vcc, s35, v84
	s_nop 1
	v_cndmask_b32_e32 v84, v84, v85, vcc
	v_sqrt_f32_e32 v85, v84
	s_nop 0
	v_add_u32_e32 v86, -1, v85
	v_add_u32_e32 v91, 1, v85
	v_fma_f32 v89, -v86, v85, v84
	v_fma_f32 v90, -v91, v85, v84
	v_cmp_ge_f32_e64 s[12:13], 0, v89
	s_nop 1
	v_cndmask_b32_e64 v85, v85, v86, s[12:13]
	v_cmp_lt_f32_e64 s[12:13], 0, v90
	s_nop 1
	v_cndmask_b32_e64 v85, v85, v91, s[12:13]
	v_mul_f32_e32 v86, 0x37800000, v85
	v_cndmask_b32_e32 v85, v85, v86, vcc
	v_cmp_class_f32_e32 vcc, v84, v109
	s_nop 1
	v_cndmask_b32_e32 v84, v85, v84, vcc
	v_div_scale_f32 v88, s[12:13], v84, v84, 1.0
	v_rcp_f32_e32 v89, v88
	v_div_scale_f32 v90, vcc, 1.0, v84, 1.0
	s_nop 0
	v_fma_f32 v91, -v88, v89, 1.0
	v_fmac_f32_e32 v89, v91, v89
	v_mul_f32_e32 v91, v90, v89
	v_fma_f32 v92, -v88, v91, v90
	v_fmac_f32_e32 v91, v92, v89
	v_fma_f32 v88, -v88, v91, v90
	v_div_fmas_f32 v88, v88, v89, v91
	v_div_fixup_f32 v88, v88, v84, 1.0
	v_pk_mul_f32 v[48:49], v[88:89], v[48:49] op_sel_hi:[0,1]
	v_pk_mul_f32 v[50:51], v[88:89], v[50:51] op_sel_hi:[0,1]
	v_pk_mul_f32 v[52:53], v[88:89], v[52:53] op_sel_hi:[0,1]
	v_pk_mul_f32 v[54:55], v[88:89], v[54:55] op_sel_hi:[0,1]
	v_pk_mul_f32 v[56:57], v[88:89], v[56:57] op_sel_hi:[0,1]
	v_pk_mul_f32 v[58:59], v[88:89], v[58:59] op_sel_hi:[0,1]
	v_pk_mul_f32 v[60:61], v[88:89], v[60:61] op_sel_hi:[0,1]
	v_pk_mul_f32 v[62:63], v[88:89], v[62:63] op_sel_hi:[0,1]
	v_pk_mul_f32 v[48:49], v[112:113], v[48:49]
	v_pk_mul_f32 v[50:51], v[114:115], v[50:51]
	global_store_dwordx4 v107, v[48:51], s[10:11]
	v_pk_mul_f32 v[52:53], v[116:117], v[52:53]
	v_pk_mul_f32 v[54:55], v[118:119], v[54:55]
	global_store_dwordx4 v107, v[52:55], s[10:11] offset:1024
	v_pk_mul_f32 v[56:57], v[120:121], v[56:57]
	v_pk_mul_f32 v[58:59], v[122:123], v[58:59]
	global_store_dwordx4 v107, v[56:59], s[10:11] offset:2048
	v_pk_mul_f32 v[60:61], v[124:125], v[60:61]
	v_pk_mul_f32 v[62:63], v[126:127], v[62:63]
	global_store_dwordx4 v107, v[60:63], s[10:11] offset:3072
.Lfin_skipB:
	s_add_i32 s2, s2, s21
	s_cmp_lt_i32 s2, 0x8000
	s_cbranch_scc1 .Lfin_loop
